# v23 + offset:128 LDS-DMA addresses in the GEMM K-loops + hand-scheduled MoE up-projection epilogue (both instruction-count reductions, bit-identical results)
# speedup vs baseline: 1.0072x; 1.0030x over previous
.LBB0_1060:
	s_add_u32 s4, s26, 0x100
	s_addc_u32 s5, s27, 0
	s_add_u32 s54, s50, s26
	s_addc_u32 s55, s51, s27
	s_cmp_eq_u32 s52, 12
	s_cselect_b64 vcc, -1, 0
	s_and_b64 s[24:25], vcc, exec
	s_cselect_b32 s53, 0, s4
	s_cselect_b32 s25, s21, s55
	s_cselect_b32 s24, s49, s54
	v_lshl_add_u64 v[18:19], v[186:187], 0, s[26:27]
	s_add_i32 m0, s33, 0xc000
	ds_read_b128 v[210:213], v203
	ds_read_b128 v[214:217], v203 offset:1024
	ds_read_b128 v[218:221], v203 offset:2048
	ds_read_b128 v[222:225], v203 offset:3072
	ds_read_b128 v[226:229], v203 offset:4096
	ds_read_b128 v[230:233], v203 offset:5120
	ds_read_b128 v[234:237], v203 offset:6144
	ds_read_b128 v[238:241], v203 offset:7168
	global_load_lds_dwordx4 v[18:19], off
	v_lshl_add_u64 v[18:19], v[184:185], 0, s[26:27]
	s_add_i32 m0, s33, 0xe000
	s_nop 0
	global_load_lds_dwordx4 v[18:19], off
	s_waitcnt lgkmcnt(8)
	s_barrier
	s_waitcnt lgkmcnt(0)
	s_waitcnt lgkmcnt(0)
	v_mfma_f32_16x16x128_f8f6f4 v[158:161], v[2:9], v[210:217], v[158:161]
	v_mfma_f32_16x16x128_f8f6f4 v[150:153], v[10:17], v[210:217], v[150:153]
	v_mfma_f32_16x16x128_f8f6f4 v[142:145], v[2:9], v[218:225], v[142:145]
	v_mfma_f32_16x16x128_f8f6f4 v[134:137], v[10:17], v[218:225], v[134:137]
	v_mfma_f32_16x16x128_f8f6f4 v[126:129], v[2:9], v[226:233], v[126:129]
	v_mfma_f32_16x16x128_f8f6f4 v[118:121], v[10:17], v[226:233], v[118:121]
	v_mfma_f32_16x16x128_f8f6f4 v[110:113], v[2:9], v[234:241], v[110:113]
	v_mfma_f32_16x16x128_f8f6f4 v[102:105], v[10:17], v[234:241], v[102:105]
	s_barrier
	s_add_i32 s26, s39, s23
	v_add_u32_e32 v30, s40, v201
	v_lshl_add_u64 v[188:189], s[24:25], 0, v[164:165]
	s_mov_b32 m0, s26
	ds_read_b128 v[18:21], v30
	ds_read_b128 v[22:25], v30 offset:1024
	ds_read_b128 v[26:29], v30 offset:2048
	ds_read_b128 v[30:33], v30 offset:3072
	global_load_lds_dwordx4 v[188:189], off
	v_lshl_add_u64 v[190:191], s[24:25], 0, v[166:167]
	s_add_i32 m0, s26, 0x2000
	s_nop 0
	global_load_lds_dwordx4 v[190:191], off
	s_barrier
	s_waitcnt lgkmcnt(0)
	s_waitcnt lgkmcnt(0)
	v_mfma_f32_16x16x128_f8f6f4 v[154:157], v[18:25], v[210:217], v[154:157]
	v_mfma_f32_16x16x128_f8f6f4 v[146:149], v[26:33], v[210:217], v[146:149]
	v_mfma_f32_16x16x128_f8f6f4 v[138:141], v[18:25], v[218:225], v[138:141]
	v_mfma_f32_16x16x128_f8f6f4 v[130:133], v[26:33], v[218:225], v[130:133]
	v_mfma_f32_16x16x128_f8f6f4 v[122:125], v[18:25], v[226:233], v[122:125]
	v_mfma_f32_16x16x128_f8f6f4 v[114:117], v[26:33], v[226:233], v[114:117]
	v_mfma_f32_16x16x128_f8f6f4 v[106:109], v[18:25], v[234:241], v[106:109]
	v_mfma_f32_16x16x128_f8f6f4 v[98:101], v[26:33], v[234:241], v[98:101]
	s_add_u32 s26, s10, s53
	s_mov_b32 m0, s33
	s_addc_u32 s27, s11, 0
	v_cndmask_b32_e32 v162, v208, v206, vcc
	s_barrier
	ds_read_b128 v[210:213], v203 offset:16384
	ds_read_b128 v[214:217], v203 offset:17408
	ds_read_b128 v[218:221], v203 offset:18432
	ds_read_b128 v[222:225], v203 offset:19456
	ds_read_b128 v[226:229], v203 offset:20480
	ds_read_b128 v[230:233], v203 offset:21504
	ds_read_b128 v[234:237], v203 offset:22528
	ds_read_b128 v[238:241], v203 offset:23552
	v_cndmask_b32_e32 v192, v178, v207, vcc
	global_load_lds_dwordx4 v162, s[26:27]
	s_mov_b32 m0, s34
	v_mov_b32_e32 v193, v163
	global_load_lds_dwordx4 v192, s[26:27]
	s_waitcnt vmcnt(10)
	s_barrier
	s_waitcnt lgkmcnt(0)
	v_lshl_add_u64 v[194:195], s[26:27], 0, v[162:163]
	v_lshl_add_u64 v[192:193], s[26:27], 0, v[192:193]
	s_waitcnt lgkmcnt(0)
	v_mfma_f32_16x16x128_f8f6f4 v[94:97], v[2:9], v[210:217], v[94:97]
	v_mfma_f32_16x16x128_f8f6f4 v[86:89], v[10:17], v[210:217], v[86:89]
	v_mfma_f32_16x16x128_f8f6f4 v[78:81], v[2:9], v[218:225], v[78:81]
	v_mfma_f32_16x16x128_f8f6f4 v[70:73], v[10:17], v[218:225], v[70:73]
	v_mfma_f32_16x16x128_f8f6f4 v[62:65], v[2:9], v[226:233], v[62:65]
	v_mfma_f32_16x16x128_f8f6f4 v[54:57], v[10:17], v[226:233], v[54:57]
	v_mfma_f32_16x16x128_f8f6f4 v[46:49], v[2:9], v[234:241], v[46:49]
	v_mfma_f32_16x16x128_f8f6f4 v[38:41], v[10:17], v[234:241], v[38:41]
	s_barrier
	v_add_u32_e32 v14, 0x18000, v201
	ds_read_b128 v[2:5], v14
	ds_read_b128 v[6:9], v14 offset:1024
	ds_read_b128 v[10:13], v14 offset:2048
	ds_read_b128 v[14:17], v14 offset:3072
	s_add_u32 s54, s24, 0x40000
	s_addc_u32 s55, s25, 0
	s_add_i32 s53, s40, s23
	v_lshl_add_u64 v[242:243], s[54:55], 0, v[164:165]
	s_mov_b32 m0, s53
	s_nop 0
	global_load_lds_dwordx4 v[242:243], off
	v_lshl_add_u64 v[242:243], s[54:55], 0, v[166:167]
	s_add_i32 m0, s53, 0x2000
	s_nop 0
	global_load_lds_dwordx4 v[242:243], off
	s_waitcnt vmcnt(6)
	s_barrier
	v_mfma_f32_16x16x128_f8f6f4 v[90:93], v[18:25], v[210:217], v[90:93]
	v_mfma_f32_16x16x128_f8f6f4 v[82:85], v[26:33], v[210:217], v[82:85]
	v_mfma_f32_16x16x128_f8f6f4 v[74:77], v[18:25], v[218:225], v[74:77]
	v_mfma_f32_16x16x128_f8f6f4 v[66:69], v[26:33], v[218:225], v[66:69]
	v_mfma_f32_16x16x128_f8f6f4 v[58:61], v[18:25], v[226:233], v[58:61]
	v_mfma_f32_16x16x128_f8f6f4 v[50:53], v[26:33], v[226:233], v[50:53]
	v_mfma_f32_16x16x128_f8f6f4 v[42:45], v[18:25], v[234:241], v[42:45]
	v_mfma_f32_16x16x128_f8f6f4 v[34:37], v[26:33], v[234:241], v[34:37]
	s_add_i32 s53, 0, 0x18000
	s_barrier
	v_cndmask_b32_e32 v172, v180, v174, vcc
	s_mov_b32 m0, s35
	v_cndmask_b32_e32 v226, v182, v176, vcc
	v_mov_b32_e32 v227, v173
	v_lshl_add_u64 v[228:229], s[26:27], 0, v[172:173]
	ds_read_b128 v[18:21], v203 offset:32768
	ds_read_b128 v[22:25], v203 offset:33792
	ds_read_b128 v[26:29], v203 offset:34816
	ds_read_b128 v[30:33], v203 offset:35840
	ds_read_b128 v[210:213], v203 offset:36864
	ds_read_b128 v[214:217], v203 offset:37888
	ds_read_b128 v[218:221], v203 offset:38912
	ds_read_b128 v[222:225], v203 offset:39936
	global_load_lds_dwordx4 v[228:229], off
	v_lshl_add_u64 v[226:227], s[26:27], 0, v[226:227]
	s_mov_b32 m0, s36
	s_nop 0
	global_load_lds_dwordx4 v[226:227], off
	s_waitcnt lgkmcnt(8)
	s_barrier
	s_waitcnt lgkmcnt(0)
	s_waitcnt lgkmcnt(0)
	v_mfma_f32_16x16x128_f8f6f4 v[158:161], v[2:9], v[18:25], v[158:161]
	v_mfma_f32_16x16x128_f8f6f4 v[150:153], v[10:17], v[18:25], v[150:153]
	v_mfma_f32_16x16x128_f8f6f4 v[142:145], v[2:9], v[26:33], v[142:145]
	v_mfma_f32_16x16x128_f8f6f4 v[134:137], v[10:17], v[26:33], v[134:137]
	v_mfma_f32_16x16x128_f8f6f4 v[126:129], v[2:9], v[210:217], v[126:129]
	v_mfma_f32_16x16x128_f8f6f4 v[118:121], v[10:17], v[210:217], v[118:121]
	v_mfma_f32_16x16x128_f8f6f4 v[110:113], v[2:9], v[218:225], v[110:113]
	v_mfma_f32_16x16x128_f8f6f4 v[102:105], v[10:17], v[218:225], v[102:105]
	s_barrier
	s_add_i32 s26, 0, 0x1c000
	s_add_i32 s27, s53, s23
	v_add_u32_e32 v162, s26, v201
	s_add_i32 m0, s27, 0xffffff80
	ds_read_b128 v[226:229], v162
	ds_read_b128 v[230:233], v162 offset:1024
	ds_read_b128 v[234:237], v162 offset:2048
	ds_read_b128 v[238:241], v162 offset:3072
	global_load_lds_dwordx4 v[188:189], off offset:128
	s_add_i32 m0, s27, 0x1f80
	s_nop 0
	global_load_lds_dwordx4 v[190:191], off offset:128
	s_barrier
	s_waitcnt lgkmcnt(0)
	s_waitcnt lgkmcnt(0)
	v_mfma_f32_16x16x128_f8f6f4 v[154:157], v[226:233], v[18:25], v[154:157]
	v_mfma_f32_16x16x128_f8f6f4 v[146:149], v[234:241], v[18:25], v[146:149]
	v_mfma_f32_16x16x128_f8f6f4 v[138:141], v[226:233], v[26:33], v[138:141]
	v_mfma_f32_16x16x128_f8f6f4 v[130:133], v[234:241], v[26:33], v[130:133]
	v_mfma_f32_16x16x128_f8f6f4 v[122:125], v[226:233], v[210:217], v[122:125]
	v_mfma_f32_16x16x128_f8f6f4 v[114:117], v[234:241], v[210:217], v[114:117]
	v_mfma_f32_16x16x128_f8f6f4 v[106:109], v[226:233], v[218:225], v[106:109]
	v_mfma_f32_16x16x128_f8f6f4 v[98:101], v[234:241], v[218:225], v[98:101]
	s_add_i32 m0, s37, 0xffffff80
	s_barrier
	ds_read_b128 v[18:21], v203 offset:49152
	ds_read_b128 v[22:25], v203 offset:50176
	ds_read_b128 v[26:29], v203 offset:51200
	ds_read_b128 v[30:33], v203 offset:52224
	ds_read_b128 v[210:213], v203 offset:53248
	ds_read_b128 v[214:217], v203 offset:54272
	ds_read_b128 v[218:221], v203 offset:55296
	ds_read_b128 v[222:225], v203 offset:56320
	global_load_lds_dwordx4 v[194:195], off offset:128
	s_add_i32 m0, s38, 0xffffff80
	s_nop 0
	global_load_lds_dwordx4 v[192:193], off offset:128
	s_waitcnt vmcnt(10)
	s_barrier
	s_waitcnt lgkmcnt(0)
	s_waitcnt lgkmcnt(0)
	v_mfma_f32_16x16x128_f8f6f4 v[94:97], v[2:9], v[18:25], v[94:97]
	v_mfma_f32_16x16x128_f8f6f4 v[86:89], v[10:17], v[18:25], v[86:89]
	v_mfma_f32_16x16x128_f8f6f4 v[78:81], v[2:9], v[26:33], v[78:81]
	v_mfma_f32_16x16x128_f8f6f4 v[70:73], v[10:17], v[26:33], v[70:73]
	v_mfma_f32_16x16x128_f8f6f4 v[62:65], v[2:9], v[210:217], v[62:65]
	v_mfma_f32_16x16x128_f8f6f4 v[54:57], v[10:17], v[210:217], v[54:57]
	v_mfma_f32_16x16x128_f8f6f4 v[46:49], v[2:9], v[218:225], v[46:49]
	v_mfma_f32_16x16x128_f8f6f4 v[38:41], v[10:17], v[218:225], v[38:41]
	s_barrier
	v_add_u32_e32 v14, s39, v201
	ds_read_b128 v[2:5], v14
	ds_read_b128 v[6:9], v14 offset:1024
	ds_read_b128 v[10:13], v14 offset:2048
	ds_read_b128 v[14:17], v14 offset:3072
	s_add_u32 s24, s24, 0x40080
	s_addc_u32 s25, s25, 0
	s_add_i32 s26, s26, s23
	v_lshl_add_u64 v[242:243], s[24:25], 0, v[164:165]
	s_mov_b32 m0, s26
	s_nop 0
	global_load_lds_dwordx4 v[242:243], off
	v_lshl_add_u64 v[242:243], s[24:25], 0, v[166:167]
	s_add_i32 m0, s26, 0x2000
	s_nop 0
	global_load_lds_dwordx4 v[242:243], off
	s_waitcnt vmcnt(6)
	s_barrier
	v_mfma_f32_16x16x128_f8f6f4 v[90:93], v[226:233], v[18:25], v[90:93]
	v_mfma_f32_16x16x128_f8f6f4 v[82:85], v[234:241], v[18:25], v[82:85]
	v_mfma_f32_16x16x128_f8f6f4 v[74:77], v[226:233], v[26:33], v[74:77]
	v_mfma_f32_16x16x128_f8f6f4 v[66:69], v[234:241], v[26:33], v[66:69]
	v_mfma_f32_16x16x128_f8f6f4 v[58:61], v[226:233], v[210:217], v[58:61]
	v_mfma_f32_16x16x128_f8f6f4 v[50:53], v[234:241], v[210:217], v[50:53]
	v_mfma_f32_16x16x128_f8f6f4 v[42:45], v[226:233], v[218:225], v[42:45]
	v_mfma_f32_16x16x128_f8f6f4 v[34:37], v[234:241], v[218:225], v[34:37]
	s_add_i32 s52, s52, 2
	s_cmp_gt_u32 s52, 13
	s_mov_b64 s[26:27], s[4:5]
	s_barrier
	s_cbranch_scc0 .LBB0_1060
	s_waitcnt lgkmcnt(0)
	v_lshl_add_u32 v4, s48, 8, v179
	s_lshl_b32 s4, s22, 7
	v_ashrrev_i32_e32 v5, 31, v4
	s_and_b32 s4, s4, 0x780
	v_lshlrev_b64 v[2:3], 11, v[4:5]
	v_or_b32_e32 v162, s4, v202
	v_lshl_add_u64 v[2:3], s[12:13], 0, v[2:3]
	v_lshl_add_u64 v[2:3], v[2:3], 0, v[162:163]
	s_nop 15
	s_nop 15
	v_mul_f32_e32 v6, 0xbcb8aa3b, v158
	v_mul_f32_e32 v7, 0xbcb8aa3b, v159
	v_mul_f32_e32 v8, 0xbcb8aa3b, v160
	v_mul_f32_e32 v9, 0xbcb8aa3b, v161
	v_mul_f32_e32 v10, 0xbcb8aa3b, v150
	v_mul_f32_e32 v11, 0xbcb8aa3b, v151
	v_mul_f32_e32 v12, 0xbcb8aa3b, v152
	v_mul_f32_e32 v13, 0xbcb8aa3b, v153
	v_exp_f32_e32 v6, v6
	v_exp_f32_e32 v7, v7
	v_exp_f32_e32 v8, v8
	v_exp_f32_e32 v9, v9
	v_exp_f32_e32 v10, v10
	v_exp_f32_e32 v11, v11
	v_exp_f32_e32 v12, v12
	v_exp_f32_e32 v13, v13
	v_mul_f32_e32 v158, v158, v154
	v_mul_f32_e32 v159, v159, v155
	v_mul_f32_e32 v160, v160, v156
	v_mul_f32_e32 v161, v161, v157
	v_mul_f32_e32 v150, v150, v146
	v_mul_f32_e32 v151, v151, v147
	v_mul_f32_e32 v152, v152, v148
	v_mul_f32_e32 v153, v153, v149
	v_add_f32_e32 v6, 1.0, v6
	v_add_f32_e32 v7, 1.0, v7
	v_add_f32_e32 v8, 1.0, v8
	v_add_f32_e32 v9, 1.0, v9
	v_add_f32_e32 v10, 1.0, v10
	v_add_f32_e32 v11, 1.0, v11
	v_add_f32_e32 v12, 1.0, v12
	v_add_f32_e32 v13, 1.0, v13
	v_rcp_f32_e32 v6, v6
	v_rcp_f32_e32 v7, v7
	v_rcp_f32_e32 v8, v8
	v_rcp_f32_e32 v9, v9
	v_rcp_f32_e32 v10, v10
	v_rcp_f32_e32 v11, v11
	v_rcp_f32_e32 v12, v12
	v_rcp_f32_e32 v13, v13
	v_mul_f32_e32 v158, v6, v158
	v_mul_f32_e32 v159, v7, v159
	v_mul_f32_e32 v160, v8, v160
	v_mul_f32_e32 v161, v9, v161
	v_mul_f32_e32 v150, v10, v150
	v_mul_f32_e32 v151, v11, v151
	v_mul_f32_e32 v152, v12, v152
	v_mul_f32_e32 v153, v13, v153
	v_mul_f32_e32 v158, 0x3a800000, v158
	v_mul_f32_e32 v159, 0x3a800000, v159
	v_mul_f32_e32 v160, 0x3a800000, v160
	v_mul_f32_e32 v161, 0x3a800000, v161
	v_mul_f32_e32 v150, 0x3a800000, v150
	v_mul_f32_e32 v151, 0x3a800000, v151
	v_mul_f32_e32 v152, 0x3a800000, v152
	v_mul_f32_e32 v153, 0x3a800000, v153
	v_med3_f32 v158, v158, s41, v205
	v_med3_f32 v159, v159, s41, v205
	v_med3_f32 v160, v160, s41, v205
	v_med3_f32 v161, v161, s41, v205
	v_med3_f32 v150, v150, s41, v205
	v_med3_f32 v151, v151, s41, v205
	v_med3_f32 v152, v152, s41, v205
	v_med3_f32 v153, v153, s41, v205
	v_cvt_pk_fp8_f32 v14, v158, v159
	v_cvt_pk_fp8_f32 v15, v150, v151
	v_cvt_pk_fp8_f32 v14, v160, v161 op_sel:[0,0,1]
	v_cvt_pk_fp8_f32 v15, v152, v153 op_sel:[0,0,1]
	s_nop 0
	global_store_dwordx2 v[2:3], v[14:15], off
	v_mul_f32_e32 v6, 0xbcb8aa3b, v142
	v_mul_f32_e32 v7, 0xbcb8aa3b, v143
	v_mul_f32_e32 v8, 0xbcb8aa3b, v144
	v_mul_f32_e32 v9, 0xbcb8aa3b, v145
	v_mul_f32_e32 v10, 0xbcb8aa3b, v134
	v_mul_f32_e32 v11, 0xbcb8aa3b, v135
	v_mul_f32_e32 v12, 0xbcb8aa3b, v136
	v_mul_f32_e32 v13, 0xbcb8aa3b, v137
	v_exp_f32_e32 v6, v6
	v_exp_f32_e32 v7, v7
	v_exp_f32_e32 v8, v8
	v_exp_f32_e32 v9, v9
	v_exp_f32_e32 v10, v10
	v_exp_f32_e32 v11, v11
	v_exp_f32_e32 v12, v12
	v_exp_f32_e32 v13, v13
	v_mul_f32_e32 v142, v142, v138
	v_mul_f32_e32 v143, v143, v139
	v_mul_f32_e32 v144, v144, v140
	v_mul_f32_e32 v145, v145, v141
	v_mul_f32_e32 v134, v134, v130
	v_mul_f32_e32 v135, v135, v131
	v_mul_f32_e32 v136, v136, v132
	v_mul_f32_e32 v137, v137, v133
	v_add_f32_e32 v6, 1.0, v6
	v_add_f32_e32 v7, 1.0, v7
	v_add_f32_e32 v8, 1.0, v8
	v_add_f32_e32 v9, 1.0, v9
	v_add_f32_e32 v10, 1.0, v10
	v_add_f32_e32 v11, 1.0, v11
	v_add_f32_e32 v12, 1.0, v12
	v_add_f32_e32 v13, 1.0, v13
	v_rcp_f32_e32 v6, v6
	v_rcp_f32_e32 v7, v7
	v_rcp_f32_e32 v8, v8
	v_rcp_f32_e32 v9, v9
	v_rcp_f32_e32 v10, v10
	v_rcp_f32_e32 v11, v11
	v_rcp_f32_e32 v12, v12
	v_rcp_f32_e32 v13, v13
	v_add_co_u32_e32 v4, vcc, 0x8000, v2
	v_mul_f32_e32 v142, v6, v142
	v_mul_f32_e32 v143, v7, v143
	v_mul_f32_e32 v144, v8, v144
	v_mul_f32_e32 v145, v9, v145
	v_mul_f32_e32 v134, v10, v134
	v_mul_f32_e32 v135, v11, v135
	v_mul_f32_e32 v136, v12, v136
	v_mul_f32_e32 v137, v13, v137
	v_addc_co_u32_e32 v5, vcc, 0, v3, vcc
	v_mul_f32_e32 v142, 0x3a800000, v142
	v_mul_f32_e32 v143, 0x3a800000, v143
	v_mul_f32_e32 v144, 0x3a800000, v144
	v_mul_f32_e32 v145, 0x3a800000, v145
	v_mul_f32_e32 v134, 0x3a800000, v134
	v_mul_f32_e32 v135, 0x3a800000, v135
	v_mul_f32_e32 v136, 0x3a800000, v136
	v_mul_f32_e32 v137, 0x3a800000, v137
	v_med3_f32 v142, v142, s41, v205
	v_med3_f32 v143, v143, s41, v205
	v_med3_f32 v144, v144, s41, v205
	v_med3_f32 v145, v145, s41, v205
	v_med3_f32 v134, v134, s41, v205
	v_med3_f32 v135, v135, s41, v205
	v_med3_f32 v136, v136, s41, v205
	v_med3_f32 v137, v137, s41, v205
	v_cvt_pk_fp8_f32 v16, v142, v143
	v_cvt_pk_fp8_f32 v17, v134, v135
	v_cvt_pk_fp8_f32 v16, v144, v145 op_sel:[0,0,1]
	v_cvt_pk_fp8_f32 v17, v136, v137 op_sel:[0,0,1]
	s_nop 0
	global_store_dwordx2 v[4:5], v[16:17], off
	v_mul_f32_e32 v6, 0xbcb8aa3b, v126
	v_mul_f32_e32 v7, 0xbcb8aa3b, v127
	v_mul_f32_e32 v8, 0xbcb8aa3b, v128
	v_mul_f32_e32 v9, 0xbcb8aa3b, v129
	v_mul_f32_e32 v10, 0xbcb8aa3b, v118
	v_mul_f32_e32 v11, 0xbcb8aa3b, v119
	v_mul_f32_e32 v12, 0xbcb8aa3b, v120
	v_mul_f32_e32 v13, 0xbcb8aa3b, v121
	v_exp_f32_e32 v6, v6
	v_exp_f32_e32 v7, v7
	v_exp_f32_e32 v8, v8
	v_exp_f32_e32 v9, v9
	v_exp_f32_e32 v10, v10
	v_exp_f32_e32 v11, v11
	v_exp_f32_e32 v12, v12
	v_exp_f32_e32 v13, v13
	v_mul_f32_e32 v126, v126, v122
	v_mul_f32_e32 v127, v127, v123
	v_mul_f32_e32 v128, v128, v124
	v_mul_f32_e32 v129, v129, v125
	v_mul_f32_e32 v118, v118, v114
	v_mul_f32_e32 v119, v119, v115
	v_mul_f32_e32 v120, v120, v116
	v_mul_f32_e32 v121, v121, v117
	v_add_f32_e32 v6, 1.0, v6
	v_add_f32_e32 v7, 1.0, v7
	v_add_f32_e32 v8, 1.0, v8
	v_add_f32_e32 v9, 1.0, v9
	v_add_f32_e32 v10, 1.0, v10
	v_add_f32_e32 v11, 1.0, v11
	v_add_f32_e32 v12, 1.0, v12
	v_add_f32_e32 v13, 1.0, v13
	v_rcp_f32_e32 v6, v6
	v_rcp_f32_e32 v7, v7
	v_rcp_f32_e32 v8, v8
	v_rcp_f32_e32 v9, v9
	v_rcp_f32_e32 v10, v10
	v_rcp_f32_e32 v11, v11
	v_rcp_f32_e32 v12, v12
	v_rcp_f32_e32 v13, v13
	v_add_co_u32_e32 v4, vcc, 0x10000, v2
	v_mul_f32_e32 v126, v6, v126
	v_mul_f32_e32 v127, v7, v127
	v_mul_f32_e32 v128, v8, v128
	v_mul_f32_e32 v129, v9, v129
	v_mul_f32_e32 v118, v10, v118
	v_mul_f32_e32 v119, v11, v119
	v_mul_f32_e32 v120, v12, v120
	v_mul_f32_e32 v121, v13, v121
	v_addc_co_u32_e32 v5, vcc, 0, v3, vcc
	v_mul_f32_e32 v126, 0x3a800000, v126
	v_mul_f32_e32 v127, 0x3a800000, v127
	v_mul_f32_e32 v128, 0x3a800000, v128
	v_mul_f32_e32 v129, 0x3a800000, v129
	v_mul_f32_e32 v118, 0x3a800000, v118
	v_mul_f32_e32 v119, 0x3a800000, v119
	v_mul_f32_e32 v120, 0x3a800000, v120
	v_mul_f32_e32 v121, 0x3a800000, v121
	v_med3_f32 v126, v126, s41, v205
	v_med3_f32 v127, v127, s41, v205
	v_med3_f32 v128, v128, s41, v205
	v_med3_f32 v129, v129, s41, v205
	v_med3_f32 v118, v118, s41, v205
	v_med3_f32 v119, v119, s41, v205
	v_med3_f32 v120, v120, s41, v205
	v_med3_f32 v121, v121, s41, v205
	v_cvt_pk_fp8_f32 v14, v126, v127
	v_cvt_pk_fp8_f32 v15, v118, v119
	v_cvt_pk_fp8_f32 v14, v128, v129 op_sel:[0,0,1]
	v_cvt_pk_fp8_f32 v15, v120, v121 op_sel:[0,0,1]
	s_nop 0
	global_store_dwordx2 v[4:5], v[14:15], off
	v_mul_f32_e32 v6, 0xbcb8aa3b, v110
	v_mul_f32_e32 v7, 0xbcb8aa3b, v111
	v_mul_f32_e32 v8, 0xbcb8aa3b, v112
	v_mul_f32_e32 v9, 0xbcb8aa3b, v113
	v_mul_f32_e32 v10, 0xbcb8aa3b, v102
	v_mul_f32_e32 v11, 0xbcb8aa3b, v103
	v_mul_f32_e32 v12, 0xbcb8aa3b, v104
	v_mul_f32_e32 v13, 0xbcb8aa3b, v105
	v_exp_f32_e32 v6, v6
	v_exp_f32_e32 v7, v7
	v_exp_f32_e32 v8, v8
	v_exp_f32_e32 v9, v9
	v_exp_f32_e32 v10, v10
	v_exp_f32_e32 v11, v11
	v_exp_f32_e32 v12, v12
	v_exp_f32_e32 v13, v13
	v_mul_f32_e32 v110, v110, v106
	v_mul_f32_e32 v111, v111, v107
	v_mul_f32_e32 v112, v112, v108
	v_mul_f32_e32 v113, v113, v109
	v_mul_f32_e32 v102, v102, v98
	v_mul_f32_e32 v103, v103, v99
	v_mul_f32_e32 v104, v104, v100
	v_mul_f32_e32 v105, v105, v101
	v_add_f32_e32 v6, 1.0, v6
	v_add_f32_e32 v7, 1.0, v7
	v_add_f32_e32 v8, 1.0, v8
	v_add_f32_e32 v9, 1.0, v9
	v_add_f32_e32 v10, 1.0, v10
	v_add_f32_e32 v11, 1.0, v11
	v_add_f32_e32 v12, 1.0, v12
	v_add_f32_e32 v13, 1.0, v13
	v_rcp_f32_e32 v6, v6
	v_rcp_f32_e32 v7, v7
	v_rcp_f32_e32 v8, v8
	v_rcp_f32_e32 v9, v9
	v_rcp_f32_e32 v10, v10
	v_rcp_f32_e32 v11, v11
	v_rcp_f32_e32 v12, v12
	v_rcp_f32_e32 v13, v13
	v_add_co_u32_e32 v4, vcc, 0x18000, v2
	v_mul_f32_e32 v110, v6, v110
	v_mul_f32_e32 v111, v7, v111
	v_mul_f32_e32 v112, v8, v112
	v_mul_f32_e32 v113, v9, v113
	v_mul_f32_e32 v102, v10, v102
	v_mul_f32_e32 v103, v11, v103
	v_mul_f32_e32 v104, v12, v104
	v_mul_f32_e32 v105, v13, v105
	v_addc_co_u32_e32 v5, vcc, 0, v3, vcc
	v_mul_f32_e32 v110, 0x3a800000, v110
	v_mul_f32_e32 v111, 0x3a800000, v111
	v_mul_f32_e32 v112, 0x3a800000, v112
	v_mul_f32_e32 v113, 0x3a800000, v113
	v_mul_f32_e32 v102, 0x3a800000, v102
	v_mul_f32_e32 v103, 0x3a800000, v103
	v_mul_f32_e32 v104, 0x3a800000, v104
	v_mul_f32_e32 v105, 0x3a800000, v105
	v_med3_f32 v110, v110, s41, v205
	v_med3_f32 v111, v111, s41, v205
	v_med3_f32 v112, v112, s41, v205
	v_med3_f32 v113, v113, s41, v205
	v_med3_f32 v102, v102, s41, v205
	v_med3_f32 v103, v103, s41, v205
	v_med3_f32 v104, v104, s41, v205
	v_med3_f32 v105, v105, s41, v205
	v_cvt_pk_fp8_f32 v16, v110, v111
	v_cvt_pk_fp8_f32 v17, v102, v103
	v_cvt_pk_fp8_f32 v16, v112, v113 op_sel:[0,0,1]
	v_cvt_pk_fp8_f32 v17, v104, v105 op_sel:[0,0,1]
	s_nop 0
	global_store_dwordx2 v[4:5], v[16:17], off
	v_mul_f32_e32 v6, 0xbcb8aa3b, v94
	v_mul_f32_e32 v7, 0xbcb8aa3b, v95
	v_mul_f32_e32 v8, 0xbcb8aa3b, v96
	v_mul_f32_e32 v9, 0xbcb8aa3b, v97
	v_mul_f32_e32 v10, 0xbcb8aa3b, v86
	v_mul_f32_e32 v11, 0xbcb8aa3b, v87
	v_mul_f32_e32 v12, 0xbcb8aa3b, v88
	v_mul_f32_e32 v13, 0xbcb8aa3b, v89
	v_exp_f32_e32 v6, v6
	v_exp_f32_e32 v7, v7
	v_exp_f32_e32 v8, v8
	v_exp_f32_e32 v9, v9
	v_exp_f32_e32 v10, v10
	v_exp_f32_e32 v11, v11
	v_exp_f32_e32 v12, v12
	v_exp_f32_e32 v13, v13
	v_mul_f32_e32 v94, v94, v90
	v_mul_f32_e32 v95, v95, v91
	v_mul_f32_e32 v96, v96, v92
	v_mul_f32_e32 v97, v97, v93
	v_mul_f32_e32 v86, v86, v82
	v_mul_f32_e32 v87, v87, v83
	v_mul_f32_e32 v88, v88, v84
	v_mul_f32_e32 v89, v89, v85
	v_add_f32_e32 v6, 1.0, v6
	v_add_f32_e32 v7, 1.0, v7
	v_add_f32_e32 v8, 1.0, v8
	v_add_f32_e32 v9, 1.0, v9
	v_add_f32_e32 v10, 1.0, v10
	v_add_f32_e32 v11, 1.0, v11
	v_add_f32_e32 v12, 1.0, v12
	v_add_f32_e32 v13, 1.0, v13
	v_rcp_f32_e32 v6, v6
	v_rcp_f32_e32 v7, v7
	v_rcp_f32_e32 v8, v8
	v_rcp_f32_e32 v9, v9
	v_rcp_f32_e32 v10, v10
	v_rcp_f32_e32 v11, v11
	v_rcp_f32_e32 v12, v12
	v_rcp_f32_e32 v13, v13
	v_add_co_u32_e32 v4, vcc, 0x40000, v2
	v_mul_f32_e32 v94, v6, v94
	v_mul_f32_e32 v95, v7, v95
	v_mul_f32_e32 v96, v8, v96
	v_mul_f32_e32 v97, v9, v97
	v_mul_f32_e32 v86, v10, v86
	v_mul_f32_e32 v87, v11, v87
	v_mul_f32_e32 v88, v12, v88
	v_mul_f32_e32 v89, v13, v89
	v_addc_co_u32_e32 v5, vcc, 0, v3, vcc
	v_mul_f32_e32 v94, 0x3a800000, v94
	v_mul_f32_e32 v95, 0x3a800000, v95
	v_mul_f32_e32 v96, 0x3a800000, v96
	v_mul_f32_e32 v97, 0x3a800000, v97
	v_mul_f32_e32 v86, 0x3a800000, v86
	v_mul_f32_e32 v87, 0x3a800000, v87
	v_mul_f32_e32 v88, 0x3a800000, v88
	v_mul_f32_e32 v89, 0x3a800000, v89
	v_med3_f32 v94, v94, s41, v205
	v_med3_f32 v95, v95, s41, v205
	v_med3_f32 v96, v96, s41, v205
	v_med3_f32 v97, v97, s41, v205
	v_med3_f32 v86, v86, s41, v205
	v_med3_f32 v87, v87, s41, v205
	v_med3_f32 v88, v88, s41, v205
	v_med3_f32 v89, v89, s41, v205
	v_cvt_pk_fp8_f32 v14, v94, v95
	v_cvt_pk_fp8_f32 v15, v86, v87
	v_cvt_pk_fp8_f32 v14, v96, v97 op_sel:[0,0,1]
	v_cvt_pk_fp8_f32 v15, v88, v89 op_sel:[0,0,1]
	s_nop 0
	global_store_dwordx2 v[4:5], v[14:15], off
	v_mul_f32_e32 v6, 0xbcb8aa3b, v78
	v_mul_f32_e32 v7, 0xbcb8aa3b, v79
	v_mul_f32_e32 v8, 0xbcb8aa3b, v80
	v_mul_f32_e32 v9, 0xbcb8aa3b, v81
	v_mul_f32_e32 v10, 0xbcb8aa3b, v70
	v_mul_f32_e32 v11, 0xbcb8aa3b, v71
	v_mul_f32_e32 v12, 0xbcb8aa3b, v72
	v_mul_f32_e32 v13, 0xbcb8aa3b, v73
	v_exp_f32_e32 v6, v6
	v_exp_f32_e32 v7, v7
	v_exp_f32_e32 v8, v8
	v_exp_f32_e32 v9, v9
	v_exp_f32_e32 v10, v10
	v_exp_f32_e32 v11, v11
	v_exp_f32_e32 v12, v12
	v_exp_f32_e32 v13, v13
	v_mul_f32_e32 v78, v78, v74
	v_mul_f32_e32 v79, v79, v75
	v_mul_f32_e32 v80, v80, v76
	v_mul_f32_e32 v81, v81, v77
	v_mul_f32_e32 v70, v70, v66
	v_mul_f32_e32 v71, v71, v67
	v_mul_f32_e32 v72, v72, v68
	v_mul_f32_e32 v73, v73, v69
	v_add_f32_e32 v6, 1.0, v6
	v_add_f32_e32 v7, 1.0, v7
	v_add_f32_e32 v8, 1.0, v8
	v_add_f32_e32 v9, 1.0, v9
	v_add_f32_e32 v10, 1.0, v10
	v_add_f32_e32 v11, 1.0, v11
	v_add_f32_e32 v12, 1.0, v12
	v_add_f32_e32 v13, 1.0, v13
	v_rcp_f32_e32 v6, v6
	v_rcp_f32_e32 v7, v7
	v_rcp_f32_e32 v8, v8
	v_rcp_f32_e32 v9, v9
	v_rcp_f32_e32 v10, v10
	v_rcp_f32_e32 v11, v11
	v_rcp_f32_e32 v12, v12
	v_rcp_f32_e32 v13, v13
	v_add_co_u32_e32 v4, vcc, 0x48000, v2
	v_mul_f32_e32 v78, v6, v78
	v_mul_f32_e32 v79, v7, v79
	v_mul_f32_e32 v80, v8, v80
	v_mul_f32_e32 v81, v9, v81
	v_mul_f32_e32 v70, v10, v70
	v_mul_f32_e32 v71, v11, v71
	v_mul_f32_e32 v72, v12, v72
	v_mul_f32_e32 v73, v13, v73
	v_addc_co_u32_e32 v5, vcc, 0, v3, vcc
	v_mul_f32_e32 v78, 0x3a800000, v78
	v_mul_f32_e32 v79, 0x3a800000, v79
	v_mul_f32_e32 v80, 0x3a800000, v80
	v_mul_f32_e32 v81, 0x3a800000, v81
	v_mul_f32_e32 v70, 0x3a800000, v70
	v_mul_f32_e32 v71, 0x3a800000, v71
	v_mul_f32_e32 v72, 0x3a800000, v72
	v_mul_f32_e32 v73, 0x3a800000, v73
	v_med3_f32 v78, v78, s41, v205
	v_med3_f32 v79, v79, s41, v205
	v_med3_f32 v80, v80, s41, v205
	v_med3_f32 v81, v81, s41, v205
	v_med3_f32 v70, v70, s41, v205
	v_med3_f32 v71, v71, s41, v205
	v_med3_f32 v72, v72, s41, v205
	v_med3_f32 v73, v73, s41, v205
	v_cvt_pk_fp8_f32 v16, v78, v79
	v_cvt_pk_fp8_f32 v17, v70, v71
	v_cvt_pk_fp8_f32 v16, v80, v81 op_sel:[0,0,1]
	v_cvt_pk_fp8_f32 v17, v72, v73 op_sel:[0,0,1]
	s_nop 0
	global_store_dwordx2 v[4:5], v[16:17], off
	v_mul_f32_e32 v6, 0xbcb8aa3b, v62
	v_mul_f32_e32 v7, 0xbcb8aa3b, v63
	v_mul_f32_e32 v8, 0xbcb8aa3b, v64
	v_mul_f32_e32 v9, 0xbcb8aa3b, v65
	v_mul_f32_e32 v10, 0xbcb8aa3b, v54
	v_mul_f32_e32 v11, 0xbcb8aa3b, v55
	v_mul_f32_e32 v12, 0xbcb8aa3b, v56
	v_mul_f32_e32 v13, 0xbcb8aa3b, v57
	v_exp_f32_e32 v6, v6
	v_exp_f32_e32 v7, v7
	v_exp_f32_e32 v8, v8
	v_exp_f32_e32 v9, v9
	v_exp_f32_e32 v10, v10
	v_exp_f32_e32 v11, v11
	v_exp_f32_e32 v12, v12
	v_exp_f32_e32 v13, v13
	v_mul_f32_e32 v62, v62, v58
	v_mul_f32_e32 v63, v63, v59
	v_mul_f32_e32 v64, v64, v60
	v_mul_f32_e32 v65, v65, v61
	v_mul_f32_e32 v54, v54, v50
	v_mul_f32_e32 v55, v55, v51
	v_mul_f32_e32 v56, v56, v52
	v_mul_f32_e32 v57, v57, v53
	v_add_f32_e32 v6, 1.0, v6
	v_add_f32_e32 v7, 1.0, v7
	v_add_f32_e32 v8, 1.0, v8
	v_add_f32_e32 v9, 1.0, v9
	v_add_f32_e32 v10, 1.0, v10
	v_add_f32_e32 v11, 1.0, v11
	v_add_f32_e32 v12, 1.0, v12
	v_add_f32_e32 v13, 1.0, v13
	v_rcp_f32_e32 v6, v6
	v_rcp_f32_e32 v7, v7
	v_rcp_f32_e32 v8, v8
	v_rcp_f32_e32 v9, v9
	v_rcp_f32_e32 v10, v10
	v_rcp_f32_e32 v11, v11
	v_rcp_f32_e32 v12, v12
	v_rcp_f32_e32 v13, v13
	v_add_co_u32_e32 v4, vcc, 0x50000, v2
	v_mul_f32_e32 v62, v6, v62
	v_mul_f32_e32 v63, v7, v63
	v_mul_f32_e32 v64, v8, v64
	v_mul_f32_e32 v65, v9, v65
	v_mul_f32_e32 v54, v10, v54
	v_mul_f32_e32 v55, v11, v55
	v_mul_f32_e32 v56, v12, v56
	v_mul_f32_e32 v57, v13, v57
	v_addc_co_u32_e32 v5, vcc, 0, v3, vcc
	v_mul_f32_e32 v62, 0x3a800000, v62
	v_mul_f32_e32 v63, 0x3a800000, v63
	v_mul_f32_e32 v64, 0x3a800000, v64
	v_mul_f32_e32 v65, 0x3a800000, v65
	v_mul_f32_e32 v54, 0x3a800000, v54
	v_mul_f32_e32 v55, 0x3a800000, v55
	v_mul_f32_e32 v56, 0x3a800000, v56
	v_mul_f32_e32 v57, 0x3a800000, v57
	v_med3_f32 v62, v62, s41, v205
	v_med3_f32 v63, v63, s41, v205
	v_med3_f32 v64, v64, s41, v205
	v_med3_f32 v65, v65, s41, v205
	v_med3_f32 v54, v54, s41, v205
	v_med3_f32 v55, v55, s41, v205
	v_med3_f32 v56, v56, s41, v205
	v_med3_f32 v57, v57, s41, v205
	v_cvt_pk_fp8_f32 v14, v62, v63
	v_cvt_pk_fp8_f32 v15, v54, v55
	v_cvt_pk_fp8_f32 v14, v64, v65 op_sel:[0,0,1]
	v_cvt_pk_fp8_f32 v15, v56, v57 op_sel:[0,0,1]
	s_nop 0
	global_store_dwordx2 v[4:5], v[14:15], off
	v_mul_f32_e32 v6, 0xbcb8aa3b, v46
	v_mul_f32_e32 v7, 0xbcb8aa3b, v47
	v_mul_f32_e32 v8, 0xbcb8aa3b, v48
	v_mul_f32_e32 v9, 0xbcb8aa3b, v49
	v_mul_f32_e32 v10, 0xbcb8aa3b, v38
	v_mul_f32_e32 v11, 0xbcb8aa3b, v39
	v_mul_f32_e32 v12, 0xbcb8aa3b, v40
	v_mul_f32_e32 v13, 0xbcb8aa3b, v41
	v_exp_f32_e32 v6, v6
	v_exp_f32_e32 v7, v7
	v_exp_f32_e32 v8, v8
	v_exp_f32_e32 v9, v9
	v_exp_f32_e32 v10, v10
	v_exp_f32_e32 v11, v11
	v_exp_f32_e32 v12, v12
	v_exp_f32_e32 v13, v13
	v_mul_f32_e32 v46, v46, v42
	v_mul_f32_e32 v47, v47, v43
	v_mul_f32_e32 v48, v48, v44
	v_mul_f32_e32 v49, v49, v45
	v_mul_f32_e32 v38, v38, v34
	v_mul_f32_e32 v39, v39, v35
	v_mul_f32_e32 v40, v40, v36
	v_mul_f32_e32 v41, v41, v37
	v_add_f32_e32 v6, 1.0, v6
	v_add_f32_e32 v7, 1.0, v7
	v_add_f32_e32 v8, 1.0, v8
	v_add_f32_e32 v9, 1.0, v9
	v_add_f32_e32 v10, 1.0, v10
	v_add_f32_e32 v11, 1.0, v11
	v_add_f32_e32 v12, 1.0, v12
	v_add_f32_e32 v13, 1.0, v13
	v_rcp_f32_e32 v6, v6
	v_rcp_f32_e32 v7, v7
	v_rcp_f32_e32 v8, v8
	v_rcp_f32_e32 v9, v9
	v_rcp_f32_e32 v10, v10
	v_rcp_f32_e32 v11, v11
	v_rcp_f32_e32 v12, v12
	v_rcp_f32_e32 v13, v13
	v_add_co_u32_e32 v4, vcc, 0x58000, v2
	v_mul_f32_e32 v46, v6, v46
	v_mul_f32_e32 v47, v7, v47
	v_mul_f32_e32 v48, v8, v48
	v_mul_f32_e32 v49, v9, v49
	v_mul_f32_e32 v38, v10, v38
	v_mul_f32_e32 v39, v11, v39
	v_mul_f32_e32 v40, v12, v40
	v_mul_f32_e32 v41, v13, v41
	v_addc_co_u32_e32 v5, vcc, 0, v3, vcc
	v_mul_f32_e32 v46, 0x3a800000, v46
	v_mul_f32_e32 v47, 0x3a800000, v47
	v_mul_f32_e32 v48, 0x3a800000, v48
	v_mul_f32_e32 v49, 0x3a800000, v49
	v_mul_f32_e32 v38, 0x3a800000, v38
	v_mul_f32_e32 v39, 0x3a800000, v39
	v_mul_f32_e32 v40, 0x3a800000, v40
	v_mul_f32_e32 v41, 0x3a800000, v41
	v_med3_f32 v46, v46, s41, v205
	v_med3_f32 v47, v47, s41, v205
	v_med3_f32 v48, v48, s41, v205
	v_med3_f32 v49, v49, s41, v205
	v_med3_f32 v38, v38, s41, v205
	v_med3_f32 v39, v39, s41, v205
	v_med3_f32 v40, v40, s41, v205
	v_med3_f32 v41, v41, s41, v205
	v_cvt_pk_fp8_f32 v16, v46, v47
	v_cvt_pk_fp8_f32 v17, v38, v39
	v_cvt_pk_fp8_f32 v16, v48, v49 op_sel:[0,0,1]
	v_cvt_pk_fp8_f32 v17, v40, v41 op_sel:[0,0,1]
	v_mov_b32_e32 v182, v176
	v_mov_b32_e32 v180, v174
	v_mov_b32_e32 v178, v207
	v_mov_b32_e32 v208, v206
	s_and_b64 vcc, exec, s[0:1]
	s_mov_b32 s48, s47
	s_mov_b32 s22, s20
	s_mov_b64 s[24:25], s[6:7]
	s_mov_b32 s21, s45
	global_store_dwordx2 v[4:5], v[16:17], off
	s_cbranch_vccz .LBB0_1042
	s_waitcnt vmcnt(0)
	s_cmpk_gt_u32 s19, 0xff
	s_cbranch_scc1 .LBB0_1064
	s_barrier
